# retention unit: next chunk's rope rows prefetched with the q/k/v rows (no exposed table loads at the chunk top) and group-norm weight rows hoisted out of the loop; on top of v26
# baseline (speedup 1.0000x reference)
.LBB0_834:
	s_or_b64 exec, exec, s[12:13]
	v_cvt_f32_i32_e32 v2, s1
	s_mov_b32 s16, 0xc2fc0000
	v_mov_b32_e32 v44, 0x42800000
	v_bfe_u32 v102, v0, 1, 7
	v_sub_f32_e32 v2, 0xc0a00000, v2
	v_cmp_gt_f32_e32 vcc, s16, v2
	s_and_b64 s[12:13], vcc, exec
	s_cselect_b32 s12, 0xffffffc0, 0
	v_cndmask_b32_e32 v3, 0, v44, vcc
	v_add_f32_e32 v2, v2, v3
	v_exp_f32_e32 v2, v2
	v_cmp_gt_i32_e64 s[26:27], s87, v0
	v_ashrrev_i32_e32 v103, 2, v0
	v_and_b32_e32 v31, 1, v26
	v_ldexp_f32 v2, v2, s12
	v_sub_f32_e32 v62, 1.0, v2
	s_mov_b32 s12, 0x800000
	v_cmp_gt_f32_e32 vcc, s12, v62
	s_and_b64 s[12:13], vcc, exec
	s_cselect_b32 s12, 32, 0
	v_ldexp_f32 v3, v62, s12
	v_log_f32_e32 v3, v3
	v_mov_b32_e32 v2, 0x42000000
	v_cndmask_b32_e32 v2, 0, v2, vcc
	v_mov_b64_e32 v[18:19], s[74:75]
	v_sub_f32_e32 v30, v3, v2
	v_mul_f32_e32 v2, 0x42fe0000, v30
	v_cmp_gt_f32_e32 vcc, s16, v2
	s_and_b64 s[12:13], vcc, exec
	s_cselect_b32 s12, 0xffffffc0, 0
	v_cndmask_b32_e32 v2, 0, v44, vcc
	v_fmac_f32_e32 v2, 0x42fe0000, v30
	v_exp_f32_e32 v2, v2
	s_lshl_b32 s68, s1, 6
	s_ashr_i32 s69, s68, 31
	s_lshl_b32 s18, s0, 12
	v_ldexp_f32 v66, v2, s12
	s_movk_i32 s12, 0xff
	v_cmp_lt_i32_e32 vcc, s12, v0
	v_mov_b32_e32 v0, 0x500
	v_mov_b32_e32 v2, 0x600
	v_cndmask_b32_e32 v0, v0, v2, vcc
	v_lshl_add_u64 v[2:3], v[0:1], 0, s[68:69]
	v_or_b32_e32 v0, s18, v102
	v_lshl_or_b32 v2, v31, 4, v2
	v_mad_i64_i32 v[4:5], s[12:13], v0, s2, v[18:19]
	v_add_u32_e32 v0, s18, v103
	v_lshlrev_b64 v[28:29], 1, v[2:3]
	v_mad_i64_i32 v[18:19], s[12:13], v0, s2, v[18:19]
	v_lshl_add_u64 v[14:15], v[4:5], 0, v[28:29]
	s_lshl_b64 s[12:13], s[68:69], 1
	v_lshlrev_b32_e32 v0, 5, v26
	global_load_dwordx4 v[2:5], v[14:15], off offset:16
	global_load_dwordx4 v[6:9], v[14:15], off
	global_load_dwordx4 v[10:13], v[14:15], off offset:80
	s_nop 0
	global_load_dwordx4 v[14:17], v[14:15], off offset:64
	v_lshl_add_u64 v[18:19], v[18:19], 0, s[12:13]
	v_and_b32_e32 v0, 0x60, v0
	v_lshl_add_u64 v[22:23], v[18:19], 0, v[0:1]
	global_load_dwordx4 v[18:21], v[22:23], off offset:3600
	s_nop 0
	global_load_dwordx4 v[22:25], v[22:23], off offset:3584
	v_lshlrev_b32_e32 v32, 4, v103
	s_ashr_i32 s1, s0, 31
	v_and_b32_e32 v32, 0x60, v32
	v_or_b32_e32 v34, 16, v0
	s_lshl_b64 s[0:1], s[0:1], 12
	v_and_b32_e32 v27, 15, v26
	v_xad_u32 v33, v32, v0, 0
	v_xad_u32 v32, v32, v34, 0
	v_lshl_add_u64 v[70:71], s[74:75], 0, v[28:29]
	s_add_u32 s0, s0, s92
	v_ashrrev_i32_e32 v28, 2, v26
	v_and_b32_e32 v34, -16, v26
	v_lshlrev_b32_e32 v35, 4, v26
	v_bfe_u32 v36, v26, 2, 2
	v_lshlrev_b32_e32 v26, 3, v26
	v_or_b32_e32 v72, s0, v27
	v_and_b32_e32 v26, 24, v26
	v_readlane_b32 s0, v252, 44
	v_cvt_f32_ubyte0_e32 v41, v102
	s_addc_u32 s1, s1, 0
	v_and_b32_e32 v74, -4, v28
	v_or_b32_e32 v38, s0, v26
	v_readlane_b32 s0, v252, 45
	v_mul_f32_e32 v42, v30, v41
	v_mov_b32_e32 v73, s1
	v_add_u32_e32 v39, s0, v74
	v_cmp_gt_f32_e64 s[0:1], s16, v42
	v_mul_f32_e64 v43, v30, -v41
	v_cmp_gt_f32_e64 s[28:29], s16, v43
	v_cndmask_b32_e64 v42, 0, v44, s[0:1]
	v_fmac_f32_e32 v42, v30, v41
	v_cndmask_b32_e64 v43, 0, v44, s[28:29]
	v_exp_f32_e32 v42, v42
	v_fma_f32 v30, v30, -v41, v43
	v_exp_f32_e32 v30, v30
	v_not_b32_e32 v43, 63
	v_cndmask_b32_e64 v41, 0, v43, s[0:1]
	s_add_i32 s41, 0, 0x10000
	v_ldexp_f32 v41, v42, v41
	v_cndmask_b32_e64 v42, 0, v43, s[28:29]
	s_lshl_b64 s[0:1], s[68:69], 2
	v_readlane_b32 s16, v254, 53
	v_ldexp_f32 v30, v30, v42
	s_add_u32 s0, s16, s0
	v_readlane_b32 s16, v254, 54
	v_ashrrev_i32_e32 v75, 31, v74
	v_mul_f32_e32 v30, 0x3e000000, v30
	s_addc_u32 s1, s16, s1
	v_lshl_add_u64 v[80:81], v[74:75], 2, s[0:1]
	v_cndmask_b32_e32 v82, v41, v30, vcc
	s_movk_i32 s0, 0x70
	v_add_u32_e32 v30, 64, v34
	v_lshlrev_b32_e32 v40, 1, v27
	v_bitop3_b32 v107, v35, v34, s0 bitop3:0x6c
	v_bitop3_b32 v108, v35, v30, s0 bitop3:0x6c
	v_readlane_b32 s0, v252, 46
	v_lshlrev_b32_e32 v104, 5, v31
	v_lshlrev_b32_e32 v43, 4, v102
	v_or_b32_e32 v52, s0, v26
	v_or_b32_e32 v53, s95, v40
	v_or_b32_e32 v40, s0, v40
	s_add_u32 s0, s74, s12
	v_or_b32_e32 v37, v74, v36
	v_and_b32_e32 v44, 0x70, v43
	v_or_b32_e32 v46, 16, v104
	v_or_b32_e32 v48, 64, v104
	v_or_b32_e32 v50, 0x50, v104
	v_and_b32_e32 v43, 0x60, v43
	v_lshlrev_b32_e32 v54, 7, v39
	v_or_b32_e32 v57, 1, v39
	v_or_b32_e32 v60, 2, v39
	v_or_b32_e32 v39, 3, v39
	s_addc_u32 s1, s75, s13
	v_or_b32_e32 v29, s92, v27
	v_xad_u32 v45, v44, v104, 0
	v_xad_u32 v47, v44, v46, 0
	v_xad_u32 v49, v44, v48, 0
	v_xad_u32 v44, v44, v50, 0
	v_xad_u32 v51, v43, v104, 0
	v_xad_u32 v46, v43, v46, 0
	v_xad_u32 v48, v43, v48, 0
	v_xad_u32 v43, v43, v50, 0
	v_sub_u32_e32 v50, v27, v74
	v_lshlrev_b32_e32 v34, 4, v37
	v_lshlrev_b32_e32 v55, 4, v28
	v_lshlrev_b32_e32 v58, 7, v57
	v_lshlrev_b32_e32 v57, 4, v57
	v_lshlrev_b32_e32 v61, 7, v60
	v_lshlrev_b32_e32 v60, 4, v60
	v_lshlrev_b32_e32 v67, 7, v39
	v_lshlrev_b32_e32 v39, 4, v39
	v_lshl_add_u64 v[84:85], s[0:1], 0, v[0:1]
	v_lshrrev_b32_e32 v0, 2, v28
	v_lshlrev_b32_e32 v28, 7, v36
	v_lshl_add_u32 v105, v29, 7, 0
	v_lshlrev_b32_e32 v29, 7, v27
	v_lshlrev_b32_e32 v30, 7, v37
	v_and_b32_e32 v35, 0x60, v34
	v_cmp_lt_i32_e64 s[28:29], -1, v50
	v_cmp_lt_i32_e64 s[30:31], 0, v50
	v_cmp_lt_i32_e64 s[34:35], 1, v50
	v_cmp_lt_i32_e64 s[36:37], 2, v50
	v_or_b32_e32 v37, 32, v26
	s_movk_i32 s16, 0x60
	v_or_b32_e32 v41, 64, v26
	v_or_b32_e32 v50, s95, v26
	v_and_b32_e32 v55, 64, v55
	v_and_b32_e32 v57, 0x50, v57
	v_and_b32_e32 v60, 0x60, v60
	v_and_b32_e32 v39, 0x70, v39
	v_lshl_or_b32 v28, v0, 9, v28
	v_lshlrev_b32_e32 v0, 6, v0
	v_lshlrev_b32_e32 v27, 2, v27
	v_mov_b32_e32 v64, 0
	v_mul_f32_e32 v68, v62, v66
	v_lshlrev_b32_e32 v31, 7, v103
	v_lshlrev_b32_e32 v42, 7, v102
	v_bitop3_b32 v37, v34, v37, s16 bitop3:0x6c
	v_bitop3_b32 v41, v34, v41, s16 bitop3:0x6c
	v_bitop3_b32 v34, v34, v26, s16 bitop3:0x4e
	v_xad_u32 v56, v55, v53, s41
	v_xad_u32 v59, v57, v53, s41
	v_xad_u32 v65, v60, v53, s41
	v_xad_u32 v53, v39, v53, s41
	v_xad_u32 v55, v55, v40, s41
	v_xad_u32 v57, v57, v40, s41
	v_xad_u32 v60, v60, v40, s41
	v_xad_u32 v39, v39, v40, s41
	v_xad_u32 v38, v35, v38, 0
	v_xad_u32 v40, v35, v50, 0
	v_xad_u32 v35, v35, v52, 0
	v_bitop3_b32 v0, v0, s16, v27 bitop3:0xc8
	s_movk_i32 s0, 0x4000
	s_mov_b32 s40, 0
	v_add_u32_e32 v106, s41, v29
	v_mov_b32_e32 v76, v68
	v_mov_b32_e32 v77, v68
	v_mov_b32_e32 v78, v66
	v_mov_b32_e32 v79, v66
	v_mov_b32_e32 v63, v62
	v_mov_b32_e32 v83, v82
	v_or_b32_e32 v109, v28, v34
	v_or_b32_e32 v110, v28, v41
	v_or_b32_e32 v111, v28, v37
	v_or3_b32 v112, v28, v0, v26
	v_add3_u32 v113, v108, v29, s0
	v_add3_u32 v114, v107, v29, s0
	v_add_u32_e32 v115, v51, v42
	v_add_u32_e32 v116, v46, v42
	v_add_u32_e32 v117, v48, v42
	v_add_u32_e32 v118, v43, v42
	v_add_u32_e32 v119, v33, v31
	v_add_u32_e32 v120, v32, v31
	v_add_u32_e32 v121, v38, v30
	v_add_u32_e32 v122, v40, v30
	v_add_u32_e32 v123, v35, v30
	v_add_u32_e32 v124, v56, v54
	v_add_u32_e32 v125, v59, v58
	v_add_u32_e32 v126, v65, v61
	v_add_u32_e32 v127, v53, v67
	v_add_u32_e32 v128, v55, v54
	v_add_u32_e32 v129, v57, v58
	v_add_u32_e32 v130, v60, v61
	v_add_u32_e32 v131, v39, v67
	v_add_u32_e32 v132, v45, v42
	v_add_u32_e32 v133, v47, v42
	v_add_u32_e32 v134, v49, v42
	v_add_u32_e32 v135, v44, v42
	v_mov_b32_e32 v65, v64
	v_mov_b32_e32 v86, v64
	v_mov_b32_e32 v87, v64
	v_mov_b32_e32 v88, v64
	v_mov_b32_e32 v89, v64
	v_mov_b32_e32 v90, v64
	v_mov_b32_e32 v91, v64
	v_lshl_or_b32 v208, v102, 6, v104
	v_mov_b32_e32 v209, 0
	v_lshl_add_u64 v[208:209], v[208:209], 2, s[24:25]
	global_load_dwordx4 v[172:175], v[208:209], off
	global_load_dwordx4 v[176:179], v[208:209], off offset:16
	global_load_dwordx4 v[180:183], v[208:209], off offset:32
	global_load_dwordx4 v[184:187], v[208:209], off offset:48
	global_load_dwordx4 v[188:191], v[208:209], off offset:64
	global_load_dwordx4 v[192:195], v[208:209], off offset:80
	global_load_dwordx4 v[196:199], v[208:209], off offset:96
	global_load_dwordx4 v[204:207], v[208:209], off offset:112
	global_load_dwordx4 v[156:159], v[80:81], off
	global_load_dwordx4 v[160:163], v[80:81], off offset:64
	global_load_dwordx4 v[164:167], v[80:81], off offset:128
	global_load_dwordx4 v[168:171], v[80:81], off offset:192
.LBB0_835:
	s_lshl_b32 s72, s40, 7
	v_or_b32_e32 v0, s72, v102
	v_lshl_or_b32 v0, v0, 6, v104
	v_lshl_add_u64 v[50:51], v[0:1], 2, s[24:25]
	s_waitcnt vmcnt(0)
	v_mov_b64_e32 v[26:27], v[180:181]
	v_mov_b64_e32 v[28:29], v[182:183]
	v_mov_b64_e32 v[30:31], v[184:185]
	v_mov_b64_e32 v[32:33], v[186:187]
	v_mov_b64_e32 v[34:35], v[172:173]
	v_mov_b64_e32 v[36:37], v[174:175]
	v_mov_b64_e32 v[38:39], v[176:177]
	v_mov_b64_e32 v[40:41], v[178:179]
	v_lshlrev_b32_e32 v47, 16, v15
	v_lshlrev_b32_e32 v46, 16, v14
	v_lshlrev_b32_e32 v43, 16, v7
	v_lshlrev_b32_e32 v42, 16, v6
	v_and_b32_e32 v49, 0xffff0000, v15
	v_and_b32_e32 v48, 0xffff0000, v14
	v_and_b32_e32 v45, 0xffff0000, v7
	v_and_b32_e32 v44, 0xffff0000, v6
	v_lshlrev_b32_e32 v95, 16, v11
	v_lshlrev_b32_e32 v94, 16, v10
	v_lshlrev_b32_e32 v61, 16, v3
	v_lshlrev_b32_e32 v60, 16, v2
	v_and_b32_e32 v97, 0xffff0000, v11
	v_and_b32_e32 v96, 0xffff0000, v10
	v_and_b32_e32 v93, 0xffff0000, v3
	v_and_b32_e32 v92, 0xffff0000, v2
	v_mov_b32_e32 v52, v34
	v_mov_b32_e32 v53, v38
	v_pk_mul_f32 v[54:55], v[52:53], v[46:47]
	v_mov_b32_e32 v38, v35
	v_pk_fma_f32 v[34:35], v[38:39], v[42:43], v[54:55]
	v_pk_mul_f32 v[38:39], v[38:39], v[46:47]
	v_mov_b32_e32 v54, v36
	v_mov_b32_e32 v55, v40
	v_mov_b32_e32 v40, v37
	v_pk_fma_f32 v[38:39], v[52:53], v[42:43], v[38:39] neg_lo:[0,0,1] neg_hi:[0,0,1]
	v_pk_mul_f32 v[56:57], v[54:55], v[48:49]
	v_pk_mul_f32 v[42:43], v[82:83], v[38:39]
	v_pk_mul_f32 v[38:39], v[40:41], v[48:49]
	v_pk_fma_f32 v[36:37], v[40:41], v[44:45], v[56:57]
	v_pk_fma_f32 v[38:39], v[54:55], v[44:45], v[38:39] neg_lo:[0,0,1] neg_hi:[0,0,1]
	v_lshlrev_b32_e32 v53, 16, v17
	v_lshlrev_b32_e32 v52, 16, v16
	v_mov_b32_e32 v56, v26
	v_mov_b32_e32 v57, v30
	v_pk_mul_f32 v[44:45], v[82:83], v[38:39]
	v_lshlrev_b32_e32 v47, 16, v9
	v_lshlrev_b32_e32 v46, 16, v8
	v_pk_mul_f32 v[38:39], v[56:57], v[52:53]
	v_mov_b32_e32 v30, v27
	v_pk_fma_f32 v[26:27], v[30:31], v[46:47], v[38:39]
	v_and_b32_e32 v55, 0xffff0000, v17
	v_and_b32_e32 v54, 0xffff0000, v16
	v_pk_mul_f32 v[38:39], v[82:83], v[26:27]
	v_mov_b32_e32 v26, v28
	v_mov_b32_e32 v27, v32
	v_and_b32_e32 v49, 0xffff0000, v9
	v_and_b32_e32 v48, 0xffff0000, v8
	v_pk_mul_f32 v[40:41], v[26:27], v[54:55]
	v_mov_b32_e32 v32, v29
	v_pk_fma_f32 v[28:29], v[32:33], v[48:49], v[40:41]
	v_pk_mul_f32 v[36:37], v[82:83], v[36:37]
	v_pk_mul_f32 v[40:41], v[82:83], v[28:29]
	v_pk_mul_f32 v[28:29], v[30:31], v[52:53]
	v_pk_mul_f32 v[34:35], v[82:83], v[34:35]
	v_pk_fma_f32 v[28:29], v[56:57], v[46:47], v[28:29] neg_lo:[0,0,1] neg_hi:[0,0,1]
	s_nop 0
	v_pk_mul_f32 v[46:47], v[82:83], v[28:29]
	v_pk_mul_f32 v[28:29], v[32:33], v[54:55]
	s_nop 0
	v_pk_fma_f32 v[26:27], v[26:27], v[48:49], v[28:29] neg_lo:[0,0,1] neg_hi:[0,0,1]
	s_nop 0
	v_pk_mul_f32 v[48:49], v[82:83], v[26:27]
	v_mov_b64_e32 v[30:31], v[196:197]
	v_mov_b64_e32 v[32:33], v[198:199]
	v_mov_b64_e32 v[26:27], v[204:205]
	v_mov_b64_e32 v[28:29], v[206:207]
	v_mov_b64_e32 v[52:53], v[188:189]
	v_mov_b64_e32 v[54:55], v[190:191]
	v_mov_b64_e32 v[56:57], v[192:193]
	v_mov_b64_e32 v[58:59], v[194:195]
	v_bfe_u32 v0, v49, 16, 1
	v_add3_u32 v0, v49, v0, s39
	s_waitcnt vmcnt(1)
	v_mov_b32_e32 v98, v52
	s_waitcnt vmcnt(0)
	v_mov_b32_e32 v99, v56
	v_pk_mul_f32 v[50:51], v[98:99], v[94:95]
	v_mov_b32_e32 v56, v53
	v_mov_b32_e32 v100, v54
	v_mov_b32_e32 v101, v58
	v_mov_b32_e32 v58, v55
	v_pk_fma_f32 v[50:51], v[56:57], v[60:61], v[50:51]
	v_pk_mul_f32 v[52:53], v[100:101], v[96:97]
	v_pk_mul_f32 v[54:55], v[56:57], v[94:95]
	v_pk_mul_f32 v[56:57], v[58:59], v[96:97]
	v_pk_fma_f32 v[52:53], v[58:59], v[92:93], v[52:53]
	v_pk_fma_f32 v[56:57], v[100:101], v[92:93], v[56:57] neg_lo:[0,0,1] neg_hi:[0,0,1]
	v_lshlrev_b32_e32 v93, 16, v13
	v_lshlrev_b32_e32 v92, 16, v12
	v_mov_b32_e32 v96, v30
	v_mov_b32_e32 v97, v26
	v_pk_fma_f32 v[54:55], v[98:99], v[60:61], v[54:55] neg_lo:[0,0,1] neg_hi:[0,0,1]
	v_lshlrev_b32_e32 v59, 16, v5
	v_lshlrev_b32_e32 v58, 16, v4
	v_pk_mul_f32 v[98:99], v[96:97], v[92:93]
	v_mov_b32_e32 v26, v31
	v_pk_fma_f32 v[30:31], v[26:27], v[58:59], v[98:99]
	v_and_b32_e32 v95, 0xffff0000, v13
	v_and_b32_e32 v94, 0xffff0000, v12
	v_pk_mul_f32 v[98:99], v[82:83], v[30:31]
	v_mov_b32_e32 v30, v32
	v_mov_b32_e32 v31, v28
	v_and_b32_e32 v61, 0xffff0000, v5
	v_and_b32_e32 v60, 0xffff0000, v4
	v_pk_mul_f32 v[100:101], v[30:31], v[94:95]
	v_mov_b32_e32 v28, v33
	v_pk_mul_f32 v[26:27], v[26:27], v[92:93]
	v_pk_fma_f32 v[32:33], v[28:29], v[60:61], v[100:101]
	v_pk_fma_f32 v[26:27], v[96:97], v[58:59], v[26:27] neg_lo:[0,0,1] neg_hi:[0,0,1]
	v_pk_mul_f32 v[100:101], v[82:83], v[32:33]
	v_pk_mul_f32 v[32:33], v[82:83], v[26:27]
	v_pk_mul_f32 v[26:27], v[28:29], v[94:95]
	v_bfe_u32 v28, v44, 16, 1
	v_pk_fma_f32 v[26:27], v[30:31], v[60:61], v[26:27] neg_lo:[0,0,1] neg_hi:[0,0,1]
	v_add3_u32 v44, v44, v28, s39
	v_pk_mul_f32 v[30:31], v[82:83], v[26:27]
	v_bfe_u32 v26, v48, 16, 1
	v_bfe_u32 v27, v45, 16, 1
	v_add3_u32 v27, v45, v27, s39
	v_add3_u32 v26, v48, v26, s39
	v_bfe_u32 v28, v42, 16, 1
	v_bfe_u32 v29, v43, 16, 1
	v_bfe_u32 v45, v46, 16, 1
	v_bfe_u32 v48, v47, 16, 1
	v_add3_u32 v47, v47, v48, s39
	v_add3_u32 v45, v46, v45, s39
	v_add3_u32 v29, v43, v29, s39
	v_add3_u32 v28, v42, v28, s39
	v_lshrrev_b32_e32 v42, 16, v28
	v_lshrrev_b32_e32 v43, 16, v29
	v_lshrrev_b32_e32 v28, 16, v45
	v_lshrrev_b32_e32 v29, 16, v47
	v_pk_mul_f32 v[54:55], v[82:83], v[54:55]
	v_and_or_b32 v29, v0, s38, v29
	v_and_or_b32 v28, v26, s38, v28
	v_and_or_b32 v26, v44, s38, v42
	v_bfe_u32 v0, v31, 16, 1
	v_bfe_u32 v42, v30, 16, 1
	v_pk_mul_f32 v[56:57], v[82:83], v[56:57]
	v_add3_u32 v30, v30, v42, s39
	v_add3_u32 v0, v31, v0, s39
	v_bfe_u32 v31, v54, 16, 1
	v_bfe_u32 v42, v55, 16, 1
	v_bfe_u32 v45, v32, 16, 1
	v_and_or_b32 v27, v27, s38, v43
	v_bfe_u32 v43, v57, 16, 1
	v_bfe_u32 v44, v56, 16, 1
	v_bfe_u32 v46, v33, 16, 1
	v_add3_u32 v32, v32, v45, s39
	v_add3_u32 v42, v55, v42, s39
	v_add3_u32 v31, v54, v31, s39
	v_add3_u32 v44, v56, v44, s39
	v_add3_u32 v43, v57, v43, s39
	v_add3_u32 v33, v33, v46, s39
	v_lshrrev_b32_e32 v45, 16, v31
	v_lshrrev_b32_e32 v31, 16, v42
	v_lshrrev_b32_e32 v32, 16, v32
	v_lshrrev_b32_e32 v33, 16, v33
	v_and_or_b32 v32, v30, s38, v32
	v_and_or_b32 v31, v43, s38, v31
	v_and_or_b32 v30, v44, s38, v45
	v_bfe_u32 v42, v40, 16, 1
	v_bfe_u32 v43, v37, 16, 1
	v_bfe_u32 v44, v36, 16, 1
	v_and_or_b32 v33, v0, s38, v33
	v_bfe_u32 v0, v41, 16, 1
	v_add3_u32 v44, v36, v44, s39
	v_add3_u32 v43, v37, v43, s39
	v_add3_u32 v36, v40, v42, s39
	v_bfe_u32 v37, v34, 16, 1
	v_bfe_u32 v40, v35, 16, 1
	v_pk_mul_f32 v[52:53], v[82:83], v[52:53]
	v_add3_u32 v0, v41, v0, s39
	v_bfe_u32 v41, v38, 16, 1
	v_bfe_u32 v42, v39, 16, 1
	v_add3_u32 v35, v35, v40, s39
	v_add3_u32 v34, v34, v37, s39
	v_pk_mul_f32 v[50:51], v[82:83], v[50:51]
	v_add3_u32 v39, v39, v42, s39
	v_add3_u32 v38, v38, v41, s39
	v_lshrrev_b32_e32 v34, 16, v34
	v_lshrrev_b32_e32 v35, 16, v35
	v_bfe_u32 v40, v52, 16, 1
	v_lshrrev_b32_e32 v38, 16, v38
	v_lshrrev_b32_e32 v37, 16, v39
	v_and_or_b32 v35, v43, s38, v35
	v_and_or_b32 v34, v44, s38, v34
	v_add3_u32 v42, v52, v40, s39
	v_bfe_u32 v40, v50, 16, 1
	v_bfe_u32 v41, v51, 16, 1
	v_bfe_u32 v43, v98, 16, 1
	v_bfe_u32 v44, v99, 16, 1
	v_and_or_b32 v37, v0, s38, v37
	v_and_or_b32 v36, v36, s38, v38
	v_bfe_u32 v0, v101, 16, 1
	v_bfe_u32 v38, v100, 16, 1
	v_bfe_u32 v39, v53, 16, 1
	v_add3_u32 v44, v99, v44, s39
	v_add3_u32 v43, v98, v43, s39
	v_add3_u32 v41, v51, v41, s39
	v_add3_u32 v40, v50, v40, s39
	v_add3_u32 v39, v53, v39, s39
	v_add3_u32 v38, v100, v38, s39
	v_add3_u32 v0, v101, v0, s39
	v_lshrrev_b32_e32 v45, 16, v40
	v_lshrrev_b32_e32 v46, 16, v41
	v_lshrrev_b32_e32 v40, 16, v43
	v_lshrrev_b32_e32 v41, 16, v44
	v_and_or_b32 v41, v0, s38, v41
	v_and_or_b32 v40, v38, s38, v40
	v_and_or_b32 v39, v39, s38, v46
	v_and_or_b32 v38, v42, s38, v45
	s_and_saveexec_b64 s[0:1], s[26:27]
	s_xor_b64 s[0:1], exec, s[0:1]
	s_cbranch_execz .LBB0_837
	ds_write_b128 v132, v[26:29]
	ds_write_b128 v133, v[30:33]
	ds_write_b128 v134, v[34:37]
	ds_write_b128 v135, v[38:41]

.LBB0_839:
	s_or_b64 exec, exec, s[0:1]
	s_add_i32 s12, s40, 1
	s_cmp_eq_u32 s40, 31
	ds_write_b128 v119, v[22:25] offset:49152
	ds_write_b128 v120, v[18:21] offset:49152
	s_waitcnt lgkmcnt(0)
	s_barrier
	s_cbranch_scc1 .LBB0_841
	s_lshl_b32 s0, s12, 7
	s_add_i32 s13, s0, s18
	v_or_b32_e32 v0, s13, v102
	v_mad_i64_i32 v[14:15], s[0:1], v0, s2, v[70:71]
	global_load_dwordx4 v[2:5], v[14:15], off offset:16
	global_load_dwordx4 v[6:9], v[14:15], off
	global_load_dwordx4 v[10:13], v[14:15], off offset:80
	s_nop 0
	global_load_dwordx4 v[14:17], v[14:15], off offset:64
	v_add_u32_e32 v0, s13, v103
	v_mad_i64_i32 v[22:23], s[0:1], v0, s2, v[84:85]
	global_load_dwordx4 v[18:21], v[22:23], off offset:3600
	s_nop 0
	global_load_dwordx4 v[22:25], v[22:23], off offset:3584
	s_lshl_b32 s100, s12, 7
	v_or_b32_e32 v208, s100, v102
	v_lshl_or_b32 v208, v208, 6, v104
	v_mov_b32_e32 v209, 0
	v_lshl_add_u64 v[208:209], v[208:209], 2, s[24:25]
	global_load_dwordx4 v[172:175], v[208:209], off
	global_load_dwordx4 v[176:179], v[208:209], off offset:16
	global_load_dwordx4 v[180:183], v[208:209], off offset:32
	global_load_dwordx4 v[184:187], v[208:209], off offset:48
	global_load_dwordx4 v[188:191], v[208:209], off offset:64
	global_load_dwordx4 v[192:195], v[208:209], off offset:80
	global_load_dwordx4 v[196:199], v[208:209], off offset:96
	global_load_dwordx4 v[204:207], v[208:209], off offset:112
